# final + phase-E converter budget 6.5 grabs (416 items per converter WG) instead of 8
# speedup vs baseline: 1.0169x; 1.0169x over previous
.LBB0_1641:
	s_mul_i32 s2, s76, 0xd760
	s_add_i32 s2, s2, 0xc300
	s_sub_i32 s82, s11, s4
	s_max_i32 s57, s50, s2
	s_mul_i32 s2, s82, 0x1a0
	s_add_i32 s2, s2, s57
	s_min_i32 s50, s2, 0x34920
	s_cmp_lt_i32 s74, 0
	s_mov_b64 s[2:3], -1
	s_cbranch_scc0 .LBB0_2087
	s_ashr_i32 s9, s10, 6
	s_not_b32 s83, s74
	s_lshl_b32 s3, s9, 3
	s_lshl_b32 s2, s83, 6
	s_add_i32 s54, s57, s3
	s_add_i32 s42, s54, s2
	s_cmp_lt_i32 s42, s50
	s_cselect_b32 s77, s42, -1
	s_cmp_lt_i32 s77, 0
	v_and_b32_e32 v132, 63, v1
	s_cbranch_scc1 .LBB0_1654
	s_mul_hi_u32 s2, s77, 0x9824d8ed
	s_lshr_b32 s2, s2, 15
	s_mul_i32 s3, s2, 0xd760
	s_sub_i32 s24, s77, s3
	s_cmpk_gt_u32 s24, 0xc2ff
	s_mov_b64 s[20:21], -1
	s_cbranch_scc0 .LBB0_1675
	s_add_i32 s20, s2, 1
	s_add_i32 s3, s24, 0xffff3d00
	s_cmpk_lt_u32 s3, 0x1400
	s_cselect_b32 s3, s3, s24
	s_cmpk_gt_u32 s3, 0xbff
	s_mov_b64 s[22:23], -1
	s_cbranch_scc0 .LBB0_1672
	s_cmpk_gt_u32 s3, 0x13ff
	s_cbranch_scc0 .LBB0_1669
	s_add_u32 s25, s78, 0x6200000
	s_addc_u32 s26, s79, 0
	s_cmpk_gt_u32 s3, 0x93ff
	s_cbranch_scc0 .LBB0_1666
	s_add_u32 s27, s78, 0x26a00000
	s_addc_u32 s28, s79, 0
	s_cmpk_gt_u32 s3, 0xd3ff
	s_cbranch_scc0 .LBB0_1663
	s_cmpk_gt_u32 s3, 0xd5ff
	s_cbranch_scc0 .LBB0_1660
	s_cmpk_gt_u32 s3, 0xd6ff
	s_cbranch_scc0 .LBB0_1657
	s_lshl_b32 s22, s3, 5
	s_cmpk_gt_u32 s3, 0xd71f
	s_mov_b64 s[18:19], -1
	s_cbranch_scc0 .LBB0_1652
	s_mov_b32 s21, s47
	v_readlane_b32 s56, v243, 40
	s_lshl_b64 s[10:11], s[20:21], 19
	v_readlane_b32 s62, v243, 46
	v_readlane_b32 s63, v243, 47
	s_add_u32 s16, s62, s10
	s_addc_u32 s17, s63, s11
	s_lshl_b64 s[10:11], s[20:21], 18
	s_add_u32 s8, s78, s10
	s_addc_u32 s13, s79, s11
	s_add_u32 s10, s8, 0x37000000
	s_addc_u32 s11, s13, 0
	s_add_u32 s12, s8, 0x37100000
	v_readlane_b32 s58, v243, 42
	s_addc_u32 s13, s13, 0
	s_lshl_b32 s8, s20, 13
	v_readlane_b32 s59, v243, 43
	s_add_u32 s14, s58, s8
	s_addc_u32 s15, s59, 0
	s_and_b32 s8, s22, 0x7fffffc0
	v_readlane_b32 s57, v243, 41
	v_readlane_b32 s60, v243, 44
	v_readlane_b32 s61, v243, 45
	v_readlane_b32 s64, v243, 48
	v_readlane_b32 s65, v243, 49
	v_readlane_b32 s66, v243, 50
	v_readlane_b32 s67, v243, 51
	v_readlane_b32 s68, v243, 52
	v_readlane_b32 s69, v243, 53
	v_readlane_b32 s70, v243, 54
	v_readlane_b32 s71, v243, 55
	s_add_i32 s8, s8, 0xffe51c00
	s_and_b32 s89, s22, 32
	s_mov_b64 s[18:19], 0
